# host half of the MoE gate/up f32->fp6 weight conversion (experts 4-7) inside the attention phase on its idle trips (same registers as the MoE-down conversion); P0 converts experts 0-3 only
# speedup vs baseline: 1.0178x; 1.0055x over previous
; template <int MODE>
; __device__ __forceinline__ void tr_matrix6(const float* W, int nb, int K, int N, unsigned char* WT, int drows, int rot, int gw, int NGW, int lane, float wscale) {
;     const int nbn = N / 32, per = (K / 256) * nbn, total = nb * per;
;     int it = gw - rot; if (it < 0) it += NGW;
;     const int c = lane & 7, q = lane >> 3;
;     for (; it < total; it += NGW) {
;         const int e = it / per, r = it - e * per, kb = r / nbn, nbk = r - kb * nbn, n0 = nbk * 32, k0 = kb * 256;
;         const float* src = W + (size_t)e * K * N + (size_t)(k0 + 32 * q) * N + n0 + 4 * c;
;         f32x4 v[32];
; #pragma unroll
;         for (int i = 0; i < 32; ++i) v[i] = *(const f32x4*)(src + (size_t)i * N);
;         const int drow0 = (MODE == 0) ? n0 : ((n0 >> 7) * 256 + (n0 & 127) + (MODE == 2 ? 128 : 0));
;         unsigned char* dst = WT + (size_t)e * drows * K + (size_t)(drow0 + 4 * c) * K + k0 + 32 * q;
.LBB0_56:
	s_mul_hi_i32 s6, s46, 0x92492493
	s_add_i32 s6, s6, s46
	s_lshr_b32 s7, s6, 31
	s_ashr_i32 s6, s6, 10
	s_add_i32 s6, s6, s7
	s_mul_i32 s7, s6, 0xfffff900
	s_mul_i32 s8, s6, 0x700
	s_mul_hi_i32 s9, s6, 0x3800000
	s_mul_i32 s10, s6, 0x3800000
	s_mul_hi_i32 s12, s6, 0x1c00000
	s_mul_i32 s13, s6, 0x1c00000
	s_add_i32 s6, s46, s7
	s_mul_hi_i32 s7, s6, 0x92492493
	s_add_i32 s7, s7, s6
	s_lshr_b32 s6, s7, 31
	s_ashr_i32 s7, s7, 7
	s_add_i32 s6, s7, s6
	s_mul_i32 s7, s6, 0xffffff20
	s_sub_i32 s7, s7, s8
	s_add_i32 s7, s46, s7
	s_lshl_b32 s6, s6, 8
	s_lshl_b32 s8, s7, 5
	s_add_u32 s10, s22, s10
	s_addc_u32 s11, s23, s9
	v_or_b32_e32 v4, s6, v146
	v_mov_b64_e32 v[2:3], s[10:11]
	s_ashr_i32 s9, s8, 31
	s_lshl_b32 s7, s7, 6
	v_mad_i64_i32 v[2:3], s[10:11], v4, s0, v[2:3]
	s_and_b32 s18, s8, 0x60
	s_and_b32 s7, s7, 0xffffff00
	v_lshl_add_u64 v[2:3], s[8:9], 2, v[2:3]
	s_add_u32 s10, s40, s13
	v_lshl_add_u64 v[8:9], v[2:3], 0, v[148:149]
	s_addc_u32 s11, s41, s12
	s_or_b32 s8, s7, s18
	v_add_co_u32_e32 v10, vcc, s0, v8
	v_or_b32_e32 v6, s8, v132
	s_nop 0
	v_addc_co_u32_e32 v11, vcc, 0, v9, vcc
	s_mov_b32 s8, 0xe000
	v_add_co_u32_e32 v12, vcc, s8, v8
	s_mov_b32 s8, 0x15000
	s_nop 0
	v_addc_co_u32_e32 v13, vcc, 0, v9, vcc
	v_add_co_u32_e32 v16, vcc, s8, v8
	s_mov_b32 s8, 0x1c000
	s_nop 0
	v_addc_co_u32_e32 v17, vcc, 0, v9, vcc
	v_add_co_u32_e32 v20, vcc, s8, v8
	s_mov_b32 s8, 0x23000
	s_nop 0
	v_addc_co_u32_e32 v21, vcc, 0, v9, vcc
	v_add_co_u32_e32 v24, vcc, s8, v8
	s_mov_b32 s8, 0x2a000
	s_nop 0
	v_addc_co_u32_e32 v25, vcc, 0, v9, vcc
	v_add_co_u32_e32 v28, vcc, s8, v8
	s_mov_b32 s8, 0x31000
	s_nop 0
	v_addc_co_u32_e32 v29, vcc, 0, v9, vcc
	v_add_co_u32_e32 v32, vcc, s8, v8
	s_mov_b32 s8, 0x38000
	s_nop 0
	v_addc_co_u32_e32 v33, vcc, 0, v9, vcc
	s_waitcnt vmcnt(15)
	v_add_co_u32_e32 v36, vcc, s8, v8
	s_mov_b32 s8, 0x3f000
	s_nop 0
	v_addc_co_u32_e32 v37, vcc, 0, v9, vcc
	s_waitcnt vmcnt(14)
	v_add_co_u32_e32 v40, vcc, s8, v8
	s_mov_b32 s8, 0x46000
	s_nop 0
	v_addc_co_u32_e32 v41, vcc, 0, v9, vcc
	s_waitcnt vmcnt(13)
	v_add_co_u32_e32 v44, vcc, s8, v8
	s_mov_b32 s8, 0x4d000
	s_nop 0
	v_addc_co_u32_e32 v45, vcc, 0, v9, vcc
	s_waitcnt vmcnt(12)
	v_add_co_u32_e32 v48, vcc, s8, v8
	s_mov_b32 s8, 0x54000
	s_nop 0
	v_addc_co_u32_e32 v49, vcc, 0, v9, vcc
	s_waitcnt vmcnt(7)
	v_add_co_u32_e32 v52, vcc, s8, v8
	s_mov_b32 s8, 0x5b000
	s_nop 0
	v_addc_co_u32_e32 v53, vcc, 0, v9, vcc
	s_waitcnt vmcnt(6)
	v_add_co_u32_e32 v56, vcc, s8, v8
	s_mov_b32 s8, 0x62000
	s_nop 0
	v_addc_co_u32_e32 v57, vcc, 0, v9, vcc
	s_waitcnt vmcnt(5)
	v_add_co_u32_e32 v60, vcc, s8, v8
	s_mov_b32 s8, 0x69000
	s_nop 0
	v_addc_co_u32_e32 v61, vcc, 0, v9, vcc
	s_waitcnt vmcnt(4)
	v_add_co_u32_e32 v64, vcc, s8, v8
	s_mov_b32 s8, 0x70000
	s_nop 0
	v_addc_co_u32_e32 v65, vcc, 0, v9, vcc
	v_add_co_u32_e32 v68, vcc, s8, v8
	s_mov_b32 s8, 0x77000
	s_nop 0
	v_addc_co_u32_e32 v69, vcc, 0, v9, vcc
	v_add_co_u32_e32 v72, vcc, s8, v8
	s_mov_b32 s8, 0x7e000
	s_nop 0
	v_addc_co_u32_e32 v73, vcc, 0, v9, vcc
	v_add_co_u32_e32 v76, vcc, s8, v8
	s_mov_b32 s8, 0x85000
	s_nop 0
	v_addc_co_u32_e32 v77, vcc, 0, v9, vcc
	v_add_co_u32_e32 v80, vcc, s8, v8
	s_mov_b32 s8, 0x8c000
	s_nop 0
	v_addc_co_u32_e32 v81, vcc, 0, v9, vcc
	v_add_co_u32_e32 v84, vcc, s8, v8
	global_load_dwordx4 v[2:5], v[8:9], off
	s_nop 0
	v_addc_co_u32_e32 v85, vcc, 0, v9, vcc
	v_add_co_u32_e32 v88, vcc, s1, v8
	v_ashrrev_i32_e32 v7, 31, v6
	s_nop 0
	v_addc_co_u32_e32 v89, vcc, 0, v9, vcc
	v_add_co_u32_e32 v92, vcc, s5, v8
	v_lshlrev_b64 v[6:7], 11, v[6:7]
	s_nop 0
	v_addc_co_u32_e32 v93, vcc, 0, v9, vcc
	v_add_co_u32_e32 v96, vcc, s14, v8
	s_ashr_i32 s7, s6, 31
	s_nop 0
	v_addc_co_u32_e32 v97, vcc, 0, v9, vcc
	v_add_co_u32_e32 v100, vcc, s15, v8
	v_lshl_add_u64 v[6:7], s[10:11], 0, v[6:7]
	s_nop 0
	v_addc_co_u32_e32 v101, vcc, 0, v9, vcc
	v_add_co_u32_e32 v104, vcc, s16, v8
	v_lshl_add_u64 v[6:7], v[6:7], 0, s[6:7]
	s_nop 0
	v_addc_co_u32_e32 v105, vcc, 0, v9, vcc
	v_add_co_u32_e32 v108, vcc, s17, v8
	v_lshl_add_u64 v[136:137], v[6:7], 0, v[146:147]
	s_nop 0
	v_addc_co_u32_e32 v109, vcc, 0, v9, vcc
	v_add_co_u32_e32 v112, vcc, s33, v8
	v_mov_b32_e32 v131, v130
	s_nop 0
	v_addc_co_u32_e32 v113, vcc, 0, v9, vcc
	v_add_co_u32_e32 v116, vcc, s38, v8
	s_add_i32 s46, s46, s72
	s_nop 0
	v_addc_co_u32_e32 v117, vcc, 0, v9, vcc
	v_add_co_u32_e32 v120, vcc, s39, v8
	s_cmpk_lt_i32 s46, 0x1c00
	s_nop 0
	v_addc_co_u32_e32 v121, vcc, 0, v9, vcc
	v_add_co_u32_e32 v124, vcc, s42, v8
	s_waitcnt vmcnt(0)
	v_mul_f32_e32 v2, 0x42b40000, v2
	v_addc_co_u32_e32 v125, vcc, 0, v9, vcc
	v_add_co_u32_e32 v128, vcc, s43, v8
	v_mul_f32_e32 v3, 0x42b40000, v3
	s_nop 0
	v_addc_co_u32_e32 v129, vcc, 0, v9, vcc
	global_load_dwordx4 v[8:11], v[10:11], off
	s_nop 0
	global_load_dwordx4 v[12:15], v[12:13], off
	s_nop 0
	global_load_dwordx4 v[16:19], v[16:17], off
	s_nop 0
	global_load_dwordx4 v[20:23], v[20:21], off
	s_nop 0
	global_load_dwordx4 v[24:27], v[24:25], off
	s_nop 0
	global_load_dwordx4 v[28:31], v[28:29], off
	s_nop 0
	global_load_dwordx4 v[32:35], v[32:33], off
	s_nop 0
	global_load_dwordx4 v[36:39], v[36:37], off
	s_nop 0
	global_load_dwordx4 v[40:43], v[40:41], off
	s_nop 0
	global_load_dwordx4 v[44:47], v[44:45], off
	s_nop 0
	global_load_dwordx4 v[48:51], v[48:49], off
	s_nop 0
	global_load_dwordx4 v[52:55], v[52:53], off
	s_nop 0
	global_load_dwordx4 v[56:59], v[56:57], off
	s_nop 0
	global_load_dwordx4 v[60:63], v[60:61], off
	s_nop 0
	global_load_dwordx4 v[64:67], v[64:65], off
	s_nop 0
	global_load_dwordx4 v[68:71], v[68:69], off
	s_nop 0
	global_load_dwordx4 v[72:75], v[72:73], off
	s_nop 0
	global_load_dwordx4 v[76:79], v[76:77], off
	s_nop 0
	global_load_dwordx4 v[80:83], v[80:81], off
	s_nop 0
	global_load_dwordx4 v[84:87], v[84:85], off
	s_nop 0
	global_load_dwordx4 v[88:91], v[88:89], off
	s_nop 0
	global_load_dwordx4 v[92:95], v[92:93], off
	s_nop 0
	global_load_dwordx4 v[96:99], v[96:97], off
	s_nop 0
	global_load_dwordx4 v[100:103], v[100:101], off
	s_nop 0
	global_load_dwordx4 v[104:107], v[104:105], off
	s_nop 0
	global_load_dwordx4 v[108:111], v[108:109], off
	s_nop 0
	global_load_dwordx4 v[112:115], v[112:113], off
	s_nop 0
	global_load_dwordx4 v[116:119], v[116:117], off
	s_nop 0
	global_load_dwordx4 v[120:123], v[120:121], off
	s_nop 0
	global_load_dwordx4 v[124:127], v[124:125], off
	s_nop 0
	global_load_dwordx4 v[138:141], v[128:129], off
	v_mul_f32_e32 v4, 0x42b40000, v4
	v_mul_f32_e32 v5, 0x42b40000, v5
	v_med3_f32 v2, v2, s44, v133
	v_add_co_u32_e32 v134, vcc, s45, v136
	s_waitcnt vmcnt(30)
; __device__ __forceinline__ v6u pk32_fp6(const float (&x)[32]) {
;     ...
;     for (int i = 0; i < 16; ++i) { a[i] = __builtin_amdgcn_fmed3f(x[i], -7.5f, 7.5f); b[i] = __builtin_amdgcn_fmed3f(x[16 + i], -7.5f, 7.5f); }
; template <int MODE>
; __device__ __forceinline__ void tr_matrix6(const float* W, int nb, int K, int N, unsigned char* WT, int drows, int rot, int gw, int NGW, int lane, float wscale) {
;     ...
;         for (int i = 0; i < 32; ++i) v[i] = *(const f32x4*)(src + (size_t)i * N);
;         const int drow0 = (MODE == 0) ? n0 : ((n0 >> 7) * 256 + (n0 & 127) + (MODE == 2 ? 128 : 0));
;         unsigned char* dst = WT + (size_t)e * drows * K + (size_t)(drow0 + 4 * c) * K + k0 + 32 * q;
; #pragma unroll
;         for (int j = 0; j < 4; ++j) { float x[32];
; #pragma unroll
;             for (int i = 0; i < 32; ++i) x[i] = v[i][j] * wscale;
;             const v6u w = pk32_fp6(x);
	v_mul_f32_e32 v6, 0x42b40000, v8
	v_mul_f32_e32 v128, 0x42b40000, v9
	v_mul_f32_e32 v129, 0x42b40000, v10
	v_mul_f32_e32 v142, 0x42b40000, v11
	s_waitcnt vmcnt(29)
	v_mul_f32_e32 v7, 0x42b40000, v12
	v_mul_f32_e32 v143, 0x42b40000, v13
	v_mul_f32_e32 v145, 0x42b40000, v14
	v_mul_f32_e32 v150, 0x42b40000, v15
	s_waitcnt vmcnt(28)
	v_mul_f32_e32 v8, 0x42b40000, v16
	v_mul_f32_e32 v151, 0x42b40000, v17
	s_waitcnt vmcnt(27)
	v_mul_f32_e32 v9, 0x42b40000, v20
	v_mul_f32_e32 v20, 0x42b40000, v22
	v_mul_f32_e32 v22, 0x42b40000, v23
	s_waitcnt vmcnt(26)
	v_mul_f32_e32 v10, 0x42b40000, v24
	v_mul_f32_e32 v23, 0x42b40000, v26
	v_mul_f32_e32 v24, 0x42b40000, v27
	s_waitcnt vmcnt(25)
	v_mul_f32_e32 v11, 0x42b40000, v28
	v_mul_f32_e32 v26, 0x42b40000, v30
	v_mul_f32_e32 v27, 0x42b40000, v31
	s_waitcnt vmcnt(24)
	v_mul_f32_e32 v12, 0x42b40000, v32
	v_mul_f32_e32 v28, 0x42b40000, v33
	v_mul_f32_e32 v30, 0x42b40000, v35
	s_waitcnt vmcnt(23)
	v_mul_f32_e32 v13, 0x42b40000, v36
	v_mul_f32_e32 v31, 0x42b40000, v37
	v_mul_f32_e32 v32, 0x42b40000, v38
	v_mul_f32_e32 v33, 0x42b40000, v39
	s_waitcnt vmcnt(22)
	v_mul_f32_e32 v14, 0x42b40000, v40
	v_mul_f32_e32 v35, 0x42b40000, v41
	v_mul_f32_e32 v155, 0x42b40000, v42
	v_mul_f32_e32 v156, 0x42b40000, v43
	s_waitcnt vmcnt(21)
	v_mul_f32_e32 v15, 0x42b40000, v44
	v_mul_f32_e32 v157, 0x42b40000, v47
	s_waitcnt vmcnt(20)
	v_mul_f32_e32 v16, 0x42b40000, v48
	v_mul_f32_e32 v37, 0x42b40000, v49
	v_mul_f32_e32 v158, 0x42b40000, v51
	s_waitcnt vmcnt(19)
	v_mul_f32_e32 v17, 0x42b40000, v52
	v_mul_f32_e32 v38, 0x42b40000, v53
	v_mul_f32_e32 v159, 0x42b40000, v55
	s_waitcnt vmcnt(18)
	v_mul_f32_e32 v39, 0x42b40000, v56
	v_mul_f32_e32 v40, 0x42b40000, v57
	v_mul_f32_e32 v47, 0x42b40000, v58
	v_mul_f32_e32 v160, 0x42b40000, v59
	s_waitcnt vmcnt(17)
	v_mul_f32_e32 v41, 0x42b40000, v60
	v_mul_f32_e32 v42, 0x42b40000, v61
	v_mul_f32_e32 v161, 0x42b40000, v63
	s_waitcnt vmcnt(16)
	v_mul_f32_e32 v43, 0x42b40000, v64
	v_mul_f32_e32 v49, 0x42b40000, v65
	s_waitcnt vmcnt(15)
	v_mul_f32_e32 v51, 0x42b40000, v68
	s_waitcnt vmcnt(14)
	v_mul_f32_e32 v53, 0x42b40000, v72
	v_mul_f32_e32 v166, 0x42b40000, v74
	v_mul_f32_e32 v167, 0x42b40000, v75
	s_waitcnt vmcnt(13)
	v_mul_f32_e32 v55, 0x42b40000, v76
	v_mul_f32_e32 v56, 0x42b40000, v77
	v_mul_f32_e32 v168, 0x42b40000, v78
	v_mul_f32_e32 v169, 0x42b40000, v79
	s_waitcnt vmcnt(12)
	v_mul_f32_e32 v57, 0x42b40000, v80
	v_mul_f32_e32 v58, 0x42b40000, v81
	s_waitcnt vmcnt(11)
	v_mul_f32_e32 v59, 0x42b40000, v84
	s_waitcnt vmcnt(10)
	v_mul_f32_e32 v61, 0x42b40000, v88
	s_waitcnt vmcnt(9)
	v_mul_f32_e32 v63, 0x42b40000, v92
	s_waitcnt vmcnt(8)
	v_mul_f32_e32 v65, 0x42b40000, v96
	s_waitcnt vmcnt(7)
	v_mul_f32_e32 v74, 0x42b40000, v100
	s_waitcnt vmcnt(6)
	v_mul_f32_e32 v75, 0x42b40000, v104
	s_waitcnt vmcnt(5)
	v_mul_f32_e32 v76, 0x42b40000, v108
	s_waitcnt vmcnt(4)
	v_mul_f32_e32 v77, 0x42b40000, v112
	s_waitcnt vmcnt(3)
	v_mul_f32_e32 v78, 0x42b40000, v116
	s_waitcnt vmcnt(2)
	v_mul_f32_e32 v79, 0x42b40000, v120
	s_waitcnt vmcnt(1)
	v_mul_f32_e32 v80, 0x42b40000, v124
	s_waitcnt vmcnt(0)
	v_mul_f32_e32 v81, 0x42b40000, v138
	v_mul_f32_e32 v152, 0x42b40000, v18
	v_mul_f32_e32 v153, 0x42b40000, v19
	v_mul_f32_e32 v19, 0x42b40000, v21
	v_mul_f32_e32 v21, 0x42b40000, v25
	v_mul_f32_e32 v25, 0x42b40000, v29
	v_mul_f32_e32 v29, 0x42b40000, v34
	v_mul_f32_e32 v36, 0x42b40000, v45
	v_mul_f32_e32 v44, 0x42b40000, v46
	v_mul_f32_e32 v45, 0x42b40000, v50
	v_mul_f32_e32 v46, 0x42b40000, v54
	v_mul_f32_e32 v48, 0x42b40000, v62
	v_mul_f32_e32 v162, 0x42b40000, v66
	v_mul_f32_e32 v163, 0x42b40000, v67
	v_mul_f32_e32 v52, 0x42b40000, v69
	v_mul_f32_e32 v164, 0x42b40000, v70
	v_mul_f32_e32 v165, 0x42b40000, v71
	v_mul_f32_e32 v54, 0x42b40000, v73
	v_mul_f32_e32 v171, 0x42b40000, v83
	v_mul_f32_e32 v60, 0x42b40000, v85
	v_mul_f32_e32 v173, 0x42b40000, v87
	v_mul_f32_e32 v62, 0x42b40000, v89
	v_mul_f32_e32 v174, 0x42b40000, v90
	v_mul_f32_e32 v175, 0x42b40000, v91
	v_mul_f32_e32 v64, 0x42b40000, v93
	v_mul_f32_e32 v176, 0x42b40000, v94
	v_mul_f32_e32 v177, 0x42b40000, v95
	v_mul_f32_e32 v89, 0x42b40000, v97
	v_mul_f32_e32 v179, 0x42b40000, v99
	v_mul_f32_e32 v90, 0x42b40000, v101
	v_mul_f32_e32 v181, 0x42b40000, v103
	v_mul_f32_e32 v91, 0x42b40000, v105
	v_mul_f32_e32 v183, 0x42b40000, v107
	v_mul_f32_e32 v92, 0x42b40000, v109
	v_mul_f32_e32 v184, 0x42b40000, v111
	v_mul_f32_e32 v93, 0x42b40000, v113
	v_mul_f32_e32 v185, 0x42b40000, v115
	v_mul_f32_e32 v94, 0x42b40000, v117
	v_mul_f32_e32 v186, 0x42b40000, v119
	v_mul_f32_e32 v95, 0x42b40000, v121
	v_mul_f32_e32 v187, 0x42b40000, v123
	v_mul_f32_e32 v96, 0x42b40000, v125
	v_mul_f32_e32 v188, 0x42b40000, v127
	v_mul_f32_e32 v97, 0x42b40000, v139
	v_mul_f32_e32 v138, 0x42b40000, v141
	v_med3_f32 v50, v3, s44, v133
	v_med3_f32 v34, v4, s44, v133
	v_med3_f32 v18, v5, s44, v133
	v_med3_f32 v3, v6, s44, v133
	v_med3_f32 v66, v51, s44, v133
	v_med3_f32 v67, v53, s44, v133
	v_med3_f32 v4, v7, s44, v133
	v_med3_f32 v68, v55, s44, v133
	v_med3_f32 v5, v8, s44, v133
	v_med3_f32 v69, v57, s44, v133
	v_med3_f32 v6, v9, s44, v133
	v_med3_f32 v70, v59, s44, v133
	v_med3_f32 v7, v10, s44, v133
	v_med3_f32 v71, v61, s44, v133
	v_med3_f32 v8, v11, s44, v133
	v_med3_f32 v72, v63, s44, v133
	v_med3_f32 v9, v12, s44, v133
	v_med3_f32 v73, v65, s44, v133
	v_med3_f32 v10, v13, s44, v133
	v_med3_f32 v74, v74, s44, v133
	v_med3_f32 v11, v14, s44, v133
	v_med3_f32 v75, v75, s44, v133
	v_med3_f32 v12, v15, s44, v133
	v_med3_f32 v76, v76, s44, v133
	v_med3_f32 v13, v16, s44, v133
	v_med3_f32 v77, v77, s44, v133
	v_med3_f32 v14, v17, s44, v133
	v_med3_f32 v78, v78, s44, v133
; __device__ __forceinline__ v6u pk32_fp6(const float (&x)[32]) {
;     ...
;     for (int i = 0; i < 16; ++i) { a[i] = __builtin_amdgcn_fmed3f(x[i], -7.5f, 7.5f); b[i] = __builtin_amdgcn_fmed3f(x[16 + i], -7.5f, 7.5f); }
;     return __builtin_amdgcn_cvt_scalef32_2xpk16_fp6_f32(a, b, 1.0f);
; template <int MODE>
; __device__ __forceinline__ void tr_matrix6(const float* W, int nb, int K, int N, unsigned char* WT, int drows, int rot, int gw, int NGW, int lane, float wscale) {
;     ...
;         for (int j = 0; j < 4; ++j) { float x[32];
; #pragma unroll
;             for (int i = 0; i < 32; ++i) x[i] = v[i][j] * wscale;
;             const v6u w = pk32_fp6(x);
;             *(u32x4*)(dst + (size_t)j * K) = (u32x4){w[0], w[1], w[2], w[3]}; *(u32x4*)(dst + (size_t)j * K + 16) = (u32x4){w[4], w[5], 0u, 0u}; }
	v_med3_f32 v15, v39, s44, v133
	v_med3_f32 v79, v79, s44, v133
	v_med3_f32 v16, v41, s44, v133
	v_med3_f32 v80, v80, s44, v133
	v_med3_f32 v17, v43, s44, v133
	v_med3_f32 v81, v81, s44, v133
	v_mul_f32_e32 v170, 0x42b40000, v82
	v_mul_f32_e32 v172, 0x42b40000, v86
	v_mul_f32_e32 v178, 0x42b40000, v98
	v_mul_f32_e32 v180, 0x42b40000, v102
	v_mul_f32_e32 v182, 0x42b40000, v106
	v_mul_f32_e32 v108, 0x42b40000, v110
	v_mul_f32_e32 v109, 0x42b40000, v114
	v_mul_f32_e32 v110, 0x42b40000, v118
	v_mul_f32_e32 v111, 0x42b40000, v122
	v_mul_f32_e32 v112, 0x42b40000, v126
	v_mul_f32_e32 v113, 0x42b40000, v140
	v_med3_f32 v51, v128, s44, v133
	v_med3_f32 v82, v52, s44, v133
	v_med3_f32 v83, v54, s44, v133
	v_med3_f32 v52, v143, s44, v133
	v_med3_f32 v84, v56, s44, v133
	v_med3_f32 v53, v151, s44, v133
	v_med3_f32 v85, v58, s44, v133
	v_med3_f32 v54, v19, s44, v133
	v_med3_f32 v86, v60, s44, v133
	v_med3_f32 v55, v21, s44, v133
	v_med3_f32 v87, v62, s44, v133
	v_med3_f32 v56, v25, s44, v133
	v_med3_f32 v88, v64, s44, v133
	v_med3_f32 v57, v28, s44, v133
	v_med3_f32 v89, v89, s44, v133
	v_med3_f32 v58, v31, s44, v133
	v_med3_f32 v90, v90, s44, v133
	v_med3_f32 v59, v35, s44, v133
	v_med3_f32 v91, v91, s44, v133
	v_med3_f32 v60, v36, s44, v133
	v_med3_f32 v92, v92, s44, v133
	v_med3_f32 v61, v37, s44, v133
	v_med3_f32 v93, v93, s44, v133
	v_med3_f32 v62, v38, s44, v133
	v_med3_f32 v94, v94, s44, v133
	v_med3_f32 v63, v40, s44, v133
	v_med3_f32 v95, v95, s44, v133
	v_med3_f32 v64, v42, s44, v133
	v_med3_f32 v96, v96, s44, v133
	v_med3_f32 v65, v49, s44, v133
	v_med3_f32 v97, v97, s44, v133
	v_med3_f32 v35, v129, s44, v133
	v_med3_f32 v38, v20, s44, v133
	v_med3_f32 v39, v23, s44, v133
	v_med3_f32 v40, v26, s44, v133
	v_med3_f32 v41, v29, s44, v133
	v_med3_f32 v42, v32, s44, v133
	v_med3_f32 v19, v142, s44, v133
	v_med3_f32 v114, v165, s44, v133
	v_med3_f32 v115, v167, s44, v133
	v_med3_f32 v20, v150, s44, v133
	v_med3_f32 v116, v169, s44, v133
	v_med3_f32 v21, v153, s44, v133
	v_med3_f32 v117, v171, s44, v133
	v_med3_f32 v22, v22, s44, v133
	v_med3_f32 v118, v173, s44, v133
	v_med3_f32 v23, v24, s44, v133
	v_med3_f32 v119, v175, s44, v133
	v_med3_f32 v24, v27, s44, v133
	v_med3_f32 v120, v177, s44, v133
	v_med3_f32 v25, v30, s44, v133
	v_med3_f32 v121, v179, s44, v133
	v_med3_f32 v26, v33, s44, v133
	v_med3_f32 v122, v181, s44, v133
	v_med3_f32 v27, v156, s44, v133
	v_med3_f32 v123, v183, s44, v133
	v_med3_f32 v28, v157, s44, v133
	v_med3_f32 v124, v184, s44, v133
	v_med3_f32 v29, v158, s44, v133
	v_med3_f32 v125, v185, s44, v133
	v_med3_f32 v30, v159, s44, v133
	v_med3_f32 v126, v186, s44, v133
	v_med3_f32 v31, v160, s44, v133
	v_med3_f32 v127, v187, s44, v133
	v_med3_f32 v32, v161, s44, v133
	v_med3_f32 v128, v188, s44, v133
	v_med3_f32 v33, v163, s44, v133
	v_med3_f32 v129, v138, s44, v133
	v_cvt_scalef32_2xpk16_fp6_f32 v[2:7], v[2:17], v[66:81], 1.0
	v_med3_f32 v98, v164, s44, v133
	v_med3_f32 v99, v166, s44, v133
	v_med3_f32 v36, v145, s44, v133
	v_med3_f32 v100, v168, s44, v133
	v_med3_f32 v37, v152, s44, v133
	v_med3_f32 v101, v170, s44, v133
	v_med3_f32 v102, v172, s44, v133
	v_med3_f32 v103, v174, s44, v133
	v_med3_f32 v104, v176, s44, v133
	v_med3_f32 v105, v178, s44, v133
	v_med3_f32 v106, v180, s44, v133
	v_med3_f32 v43, v155, s44, v133
	v_med3_f32 v107, v182, s44, v133
	v_med3_f32 v44, v44, s44, v133
	v_med3_f32 v108, v108, s44, v133
	v_med3_f32 v45, v45, s44, v133
	v_med3_f32 v109, v109, s44, v133
	v_med3_f32 v46, v46, s44, v133
	v_med3_f32 v110, v110, s44, v133
	v_med3_f32 v47, v47, s44, v133
	v_med3_f32 v111, v111, s44, v133
	v_med3_f32 v48, v48, s44, v133
	v_med3_f32 v112, v112, s44, v133
	v_med3_f32 v49, v162, s44, v133
	v_med3_f32 v113, v113, s44, v133
	v_cvt_scalef32_2xpk16_fp6_f32 v[8:13], v[50:65], v[82:97], 1.0
	v_cvt_scalef32_2xpk16_fp6_f32 v[14:19], v[18:33], v[114:129], 1.0
	v_mov_b32_e32 v128, v6
	v_mov_b32_e32 v129, v7
	v_addc_co_u32_e32 v135, vcc, 0, v137, vcc
	v_cvt_scalef32_2xpk16_fp6_f32 v[34:39], v[34:49], v[98:113], 1.0
	global_store_dwordx4 v[136:137], v[2:5], off
	global_store_dwordx4 v[136:137], v[8:11], off offset:2048
	global_store_dwordx4 v[134:135], v[34:37], off
	global_store_dwordx4 v[134:135], v[14:17], off offset:2048
	global_store_dwordx4 v[136:137], v[128:131], off offset:16
	s_nop 1
	v_mov_b32_e32 v128, v12
	v_mov_b32_e32 v129, v13
	global_store_dwordx4 v[136:137], v[128:131], off offset:2064
	s_nop 1
	v_mov_b32_e32 v128, v38
	v_mov_b32_e32 v129, v39
	global_store_dwordx4 v[134:135], v[128:131], off offset:16
	s_nop 1
	v_mov_b32_e32 v128, v18
	v_mov_b32_e32 v129, v19
	global_store_dwordx4 v[134:135], v[128:131], off offset:2064
	s_cbranch_scc1 .LBB0_56
	v_or_b32_e32 v145, 0x80, v132
	s_movk_i32 s0, 0x7000
	v_mov_b32_e32 v149, 0
	s_mov_b32 s1, 0x7e000
	s_mov_b32 s5, 0x85000
	s_mov_b32 s14, 0x8c000
	s_mov_b32 s15, 0x93000
	s_mov_b32 s16, 0x9a000
	s_mov_b32 s17, 0xa1000
	s_mov_b32 s22, 0xa8000
	s_mov_b32 s23, 0xaf000
	s_mov_b32 s33, 0xb6000
	s_mov_b32 s38, 0xbd000
	s_mov_b32 s39, 0xc4000
	s_mov_b32 s42, 0xcb000
	s_mov_b32 s43, 0xd2000
	s_mov_b32 s44, 0xd9000
	s_mov_b32 s45, 0xc0f00000
	s_movk_i32 s46, 0x1000
	v_mov_b32_e32 v155, 0x40f00000
; template <int MODE>
; __device__ __forceinline__ void tr_matrix6(const float* W, int nb, int K, int N, unsigned char* WT, int drows, int rot, int gw, int NGW, int lane, float wscale) {
;     const int nbn = N / 32, per = (K / 256) * nbn, total = nb * per;
;     int it = gw - rot; if (it < 0) it += NGW;
;     const int c = lane & 7, q = lane >> 3;
;     for (; it < total; it += NGW) {
;         const int e = it / per, r = it - e * per, kb = r / nbn, nbk = r - kb * nbn, n0 = nbk * 32, k0 = kb * 256;
;         const float* src = W + (size_t)e * K * N + (size_t)(k0 + 32 * q) * N + n0 + 4 * c;
;         f32x4 v[32];
; #pragma unroll
;         for (int i = 0; i < 32; ++i) v[i] = *(const f32x4*)(src + (size_t)i * N);
;         const int drow0 = (MODE == 0) ? n0 : ((n0 >> 7) * 256 + (n0 & 127) + (MODE == 2 ? 128 : 0));
;         unsigned char* dst = WT + (size_t)e * drows * K + (size_t)(drow0 + 4 * c) * K + k0 + 32 * q;
.LBB0_58:
	s_mul_hi_i32 s6, s3, 0x92492493
	s_add_i32 s6, s6, s3
	s_lshr_b32 s7, s6, 31
	s_ashr_i32 s6, s6, 10
	s_add_i32 s6, s6, s7
	s_mul_i32 s7, s6, 0xfffff900
	s_mul_i32 s8, s6, 0x700
	s_mul_hi_i32 s9, s6, 0x3800000
	s_mul_i32 s10, s6, 0x3800000
	s_mul_hi_i32 s12, s6, 0x1c00000
	s_mul_i32 s13, s6, 0x1c00000
	s_add_i32 s6, s3, s7
	s_mul_hi_i32 s7, s6, 0x92492493
	s_add_i32 s7, s7, s6
	s_lshr_b32 s6, s7, 31
	s_ashr_i32 s7, s7, 7
	s_add_i32 s6, s7, s6
	s_mul_i32 s7, s6, 0xffffff20
	s_sub_i32 s7, s7, s8
	s_add_i32 s7, s3, s7
	s_lshl_b32 s6, s6, 8
	s_lshl_b32 s8, s7, 5
	s_add_u32 s10, s24, s10
	s_addc_u32 s11, s25, s9
	v_or_b32_e32 v4, s6, v146
	v_mov_b64_e32 v[2:3], s[10:11]
	s_ashr_i32 s9, s8, 31
	s_lshl_b32 s7, s7, 6
	v_mad_i64_i32 v[2:3], s[10:11], v4, s0, v[2:3]
	s_and_b32 s18, s8, 0x60
	s_and_b32 s7, s7, 0xffffff00
	v_lshl_add_u64 v[2:3], s[8:9], 2, v[2:3]
	s_add_u32 s10, s40, s13
	v_lshl_add_u64 v[8:9], v[2:3], 0, v[148:149]
	s_addc_u32 s11, s41, s12
	s_or_b32 s8, s7, s18
	v_add_co_u32_e32 v10, vcc, s0, v8
	v_or_b32_e32 v6, s8, v145
	s_nop 0
	v_addc_co_u32_e32 v11, vcc, 0, v9, vcc
	s_mov_b32 s8, 0xe000
	v_add_co_u32_e32 v12, vcc, s8, v8
	s_mov_b32 s8, 0x15000
	s_nop 0
	v_addc_co_u32_e32 v13, vcc, 0, v9, vcc
	v_add_co_u32_e32 v16, vcc, s8, v8
	s_mov_b32 s8, 0x1c000
	s_nop 0
	v_addc_co_u32_e32 v17, vcc, 0, v9, vcc
	v_add_co_u32_e32 v20, vcc, s8, v8
	s_mov_b32 s8, 0x23000
	s_nop 0
	v_addc_co_u32_e32 v21, vcc, 0, v9, vcc
	v_add_co_u32_e32 v24, vcc, s8, v8
	s_mov_b32 s8, 0x2a000
	s_nop 0
	v_addc_co_u32_e32 v25, vcc, 0, v9, vcc
	v_add_co_u32_e32 v28, vcc, s8, v8
	s_mov_b32 s8, 0x31000
	s_nop 0
	v_addc_co_u32_e32 v29, vcc, 0, v9, vcc
	v_add_co_u32_e32 v32, vcc, s8, v8
	s_mov_b32 s8, 0x38000
	s_nop 0
	v_addc_co_u32_e32 v33, vcc, 0, v9, vcc
	v_add_co_u32_e32 v36, vcc, s8, v8
	s_mov_b32 s8, 0x3f000
	s_nop 0
	v_addc_co_u32_e32 v37, vcc, 0, v9, vcc
	v_add_co_u32_e32 v40, vcc, s8, v8
	s_mov_b32 s8, 0x46000
	s_nop 0
	v_addc_co_u32_e32 v41, vcc, 0, v9, vcc
	v_add_co_u32_e32 v44, vcc, s8, v8
	s_mov_b32 s8, 0x4d000
	s_nop 0
	v_addc_co_u32_e32 v45, vcc, 0, v9, vcc
	v_add_co_u32_e32 v48, vcc, s8, v8
	s_mov_b32 s8, 0x54000
	s_nop 0
	v_addc_co_u32_e32 v49, vcc, 0, v9, vcc
	v_add_co_u32_e32 v52, vcc, s8, v8
	s_mov_b32 s8, 0x5b000
	s_nop 0
	v_addc_co_u32_e32 v53, vcc, 0, v9, vcc
	v_add_co_u32_e32 v56, vcc, s8, v8
	s_mov_b32 s8, 0x62000
	s_nop 0
	v_addc_co_u32_e32 v57, vcc, 0, v9, vcc
	v_add_co_u32_e32 v60, vcc, s8, v8
	s_mov_b32 s8, 0x69000
	s_nop 0
	v_addc_co_u32_e32 v61, vcc, 0, v9, vcc
	v_add_co_u32_e32 v64, vcc, s8, v8
	s_mov_b32 s8, 0x70000
	s_nop 0
	v_addc_co_u32_e32 v65, vcc, 0, v9, vcc
	v_add_co_u32_e32 v68, vcc, s8, v8
	s_mov_b32 s8, 0x77000
	s_nop 0
	v_addc_co_u32_e32 v69, vcc, 0, v9, vcc
	v_add_co_u32_e32 v72, vcc, s8, v8
	global_load_dwordx4 v[2:5], v[8:9], off
	s_nop 0
	v_addc_co_u32_e32 v73, vcc, 0, v9, vcc
	v_add_co_u32_e32 v76, vcc, s1, v8
	v_ashrrev_i32_e32 v7, 31, v6
	s_nop 0
	v_addc_co_u32_e32 v77, vcc, 0, v9, vcc
	v_add_co_u32_e32 v80, vcc, s5, v8
	v_lshlrev_b64 v[6:7], 11, v[6:7]
	s_nop 0
	v_addc_co_u32_e32 v81, vcc, 0, v9, vcc
	v_add_co_u32_e32 v84, vcc, s14, v8
	s_ashr_i32 s7, s6, 31
	s_nop 0
	v_addc_co_u32_e32 v85, vcc, 0, v9, vcc
	v_add_co_u32_e32 v88, vcc, s15, v8
	v_lshl_add_u64 v[6:7], s[10:11], 0, v[6:7]
	s_nop 0
	v_addc_co_u32_e32 v89, vcc, 0, v9, vcc
	v_add_co_u32_e32 v92, vcc, s16, v8
	v_lshl_add_u64 v[6:7], v[6:7], 0, s[6:7]
	s_nop 0
	v_addc_co_u32_e32 v93, vcc, 0, v9, vcc
	v_add_co_u32_e32 v96, vcc, s17, v8
	v_lshl_add_u64 v[150:151], v[6:7], 0, v[146:147]
	s_nop 0
	v_addc_co_u32_e32 v97, vcc, 0, v9, vcc
	v_add_co_u32_e32 v100, vcc, s22, v8
	s_add_i32 s3, s3, s72
	s_nop 0
	v_addc_co_u32_e32 v101, vcc, 0, v9, vcc
	v_add_co_u32_e32 v104, vcc, s23, v8
	v_mov_b32_e32 v130, v149
	s_nop 0
	v_addc_co_u32_e32 v105, vcc, 0, v9, vcc
	v_add_co_u32_e32 v108, vcc, s33, v8
	v_mov_b32_e32 v131, v149
	s_nop 0
	v_addc_co_u32_e32 v109, vcc, 0, v9, vcc
	v_add_co_u32_e32 v112, vcc, s38, v8
	s_cmpk_lt_i32 s3, 0x1c00
	s_nop 0
	v_addc_co_u32_e32 v113, vcc, 0, v9, vcc
	v_add_co_u32_e32 v116, vcc, s39, v8
	v_mov_b32_e32 v134, v149
	s_nop 0
	v_addc_co_u32_e32 v117, vcc, 0, v9, vcc
	v_add_co_u32_e32 v120, vcc, s42, v8
	v_mov_b32_e32 v135, v149
	s_nop 0
	v_addc_co_u32_e32 v121, vcc, 0, v9, vcc
	v_add_co_u32_e32 v124, vcc, s43, v8
	v_mov_b32_e32 v138, v149
	s_nop 0
	v_addc_co_u32_e32 v125, vcc, 0, v9, vcc
	v_add_co_u32_e32 v128, vcc, s44, v8
	v_mov_b32_e32 v139, v149
	s_nop 0
	v_addc_co_u32_e32 v129, vcc, 0, v9, vcc
	global_load_dwordx4 v[8:11], v[10:11], off
	s_nop 0
	global_load_dwordx4 v[12:15], v[12:13], off
	s_nop 0
	global_load_dwordx4 v[16:19], v[16:17], off
	s_nop 0
	global_load_dwordx4 v[20:23], v[20:21], off
	s_nop 0
	global_load_dwordx4 v[24:27], v[24:25], off
	s_nop 0
	global_load_dwordx4 v[28:31], v[28:29], off
	s_nop 0
	global_load_dwordx4 v[32:35], v[32:33], off
	s_nop 0
	global_load_dwordx4 v[36:39], v[36:37], off
	s_nop 0
	global_load_dwordx4 v[40:43], v[40:41], off
	s_nop 0
	global_load_dwordx4 v[44:47], v[44:45], off
	s_nop 0
	global_load_dwordx4 v[48:51], v[48:49], off
	s_nop 0
	global_load_dwordx4 v[52:55], v[52:53], off
	s_nop 0
	global_load_dwordx4 v[56:59], v[56:57], off
	s_nop 0
	global_load_dwordx4 v[60:63], v[60:61], off
	s_nop 0
	global_load_dwordx4 v[64:67], v[64:65], off
	s_nop 0
	global_load_dwordx4 v[68:71], v[68:69], off
	s_nop 0
	global_load_dwordx4 v[72:75], v[72:73], off
	s_nop 0
	global_load_dwordx4 v[76:79], v[76:77], off
	s_nop 0
	global_load_dwordx4 v[80:83], v[80:81], off
	s_nop 0
	global_load_dwordx4 v[84:87], v[84:85], off
	s_nop 0
	global_load_dwordx4 v[88:91], v[88:89], off
	s_nop 0
	global_load_dwordx4 v[92:95], v[92:93], off
	s_nop 0
	global_load_dwordx4 v[96:99], v[96:97], off
	s_nop 0
	global_load_dwordx4 v[100:103], v[100:101], off
	s_nop 0
	global_load_dwordx4 v[104:107], v[104:105], off
	s_nop 0
	global_load_dwordx4 v[108:111], v[108:109], off
	s_nop 0
	global_load_dwordx4 v[112:115], v[112:113], off
	s_nop 0
	global_load_dwordx4 v[116:119], v[116:117], off
	s_nop 0
	global_load_dwordx4 v[120:123], v[120:121], off
	s_nop 0
	global_load_dwordx4 v[124:127], v[124:125], off
	s_nop 0
	global_load_dwordx4 v[156:159], v[128:129], off
	v_add_co_u32_e32 v152, vcc, s46, v150
	v_mov_b32_e32 v142, v149
	s_nop 0
	v_addc_co_u32_e32 v153, vcc, 0, v151, vcc
	v_mov_b32_e32 v143, v149
	s_waitcnt vmcnt(31)
; template <int MODE>
; __device__ __forceinline__ void tr_matrix6(const float* W, int nb, int K, int N, unsigned char* WT, int drows, int rot, int gw, int NGW, int lane, float wscale) {
;     ...
;         for (int j = 0; j < 4; ++j) { float x[32];
; #pragma unroll
;             for (int i = 0; i < 32; ++i) x[i] = v[i][j] * wscale;
;             const v6u w = pk32_fp6(x);
	v_mul_f32_e32 v2, 0x42b40000, v2
	v_mul_f32_e32 v3, 0x42b40000, v3
	v_mul_f32_e32 v4, 0x42b40000, v4
	v_mul_f32_e32 v5, 0x42b40000, v5
	v_med3_f32 v2, v2, s45, v155
	s_waitcnt vmcnt(30)
	v_mul_f32_e32 v6, 0x42b40000, v8
	s_waitcnt vmcnt(29)
	v_mul_f32_e32 v7, 0x42b40000, v12
	s_waitcnt vmcnt(28)
	v_mul_f32_e32 v8, 0x42b40000, v16
	s_waitcnt vmcnt(27)
	v_mul_f32_e32 v12, 0x42b40000, v20
	s_waitcnt vmcnt(26)
	v_mul_f32_e32 v16, 0x42b40000, v24
	s_waitcnt vmcnt(25)
	v_mul_f32_e32 v20, 0x42b40000, v28
	v_mul_f32_e32 v24, 0x42b40000, v9
	v_mul_f32_e32 v28, 0x42b40000, v10
	v_mul_f32_e32 v128, 0x42b40000, v11
	s_waitcnt vmcnt(24)
	v_mul_f32_e32 v9, 0x42b40000, v32
	v_mul_f32_e32 v32, 0x42b40000, v13
	v_mul_f32_e32 v129, 0x42b40000, v14
	v_mul_f32_e32 v132, 0x42b40000, v15
	s_waitcnt vmcnt(23)
	v_mul_f32_e32 v10, 0x42b40000, v36
	v_mul_f32_e32 v36, 0x42b40000, v17
	s_waitcnt vmcnt(22)
	v_mul_f32_e32 v11, 0x42b40000, v40
	s_waitcnt vmcnt(21)
	v_mul_f32_e32 v13, 0x42b40000, v44
	s_waitcnt vmcnt(20)
	v_mul_f32_e32 v14, 0x42b40000, v48
	s_waitcnt vmcnt(19)
	v_mul_f32_e32 v15, 0x42b40000, v52
	v_mul_f32_e32 v137, 0x42b40000, v35
	s_waitcnt vmcnt(18)
	v_mul_f32_e32 v17, 0x42b40000, v56
	v_mul_f32_e32 v35, 0x42b40000, v37
	v_mul_f32_e32 v44, 0x42b40000, v38
	v_mul_f32_e32 v140, 0x42b40000, v39
	s_waitcnt vmcnt(17)
	v_mul_f32_e32 v37, 0x42b40000, v60
	v_mul_f32_e32 v38, 0x42b40000, v41
	v_mul_f32_e32 v48, 0x42b40000, v42
	v_mul_f32_e32 v141, 0x42b40000, v43
	s_waitcnt vmcnt(16)
	v_mul_f32_e32 v39, 0x42b40000, v64
	v_mul_f32_e32 v160, 0x42b40000, v47
	s_waitcnt vmcnt(15)
	v_mul_f32_e32 v41, 0x42b40000, v68
	v_mul_f32_e32 v42, 0x42b40000, v49
	v_mul_f32_e32 v161, 0x42b40000, v51
	s_waitcnt vmcnt(14)
	v_mul_f32_e32 v43, 0x42b40000, v72
	v_mul_f32_e32 v47, 0x42b40000, v53
	v_mul_f32_e32 v49, 0x42b40000, v54
	s_waitcnt vmcnt(13)
	v_mul_f32_e32 v51, 0x42b40000, v76
	v_mul_f32_e32 v163, 0x42b40000, v58
	v_mul_f32_e32 v164, 0x42b40000, v59
	s_waitcnt vmcnt(12)
	v_mul_f32_e32 v52, 0x42b40000, v80
	v_mul_f32_e32 v165, 0x42b40000, v61
	v_mul_f32_e32 v166, 0x42b40000, v62
	s_waitcnt vmcnt(11)
	v_mul_f32_e32 v53, 0x42b40000, v84
	s_waitcnt vmcnt(10)
	v_mul_f32_e32 v54, 0x42b40000, v88
	s_waitcnt vmcnt(9)
	v_mul_f32_e32 v56, 0x42b40000, v92
	s_waitcnt vmcnt(8)
	v_mul_f32_e32 v58, 0x42b40000, v96
	v_mul_f32_e32 v59, 0x42b40000, v77
	v_mul_f32_e32 v174, 0x42b40000, v78
	v_mul_f32_e32 v175, 0x42b40000, v79
	s_waitcnt vmcnt(7)
	v_mul_f32_e32 v60, 0x42b40000, v100
	v_mul_f32_e32 v61, 0x42b40000, v81
	s_waitcnt vmcnt(6)
	v_mul_f32_e32 v62, 0x42b40000, v104
	s_waitcnt vmcnt(5)
	v_mul_f32_e32 v76, 0x42b40000, v108
	s_waitcnt vmcnt(4)
	v_mul_f32_e32 v77, 0x42b40000, v112
	s_waitcnt vmcnt(3)
	v_mul_f32_e32 v78, 0x42b40000, v116
	s_waitcnt vmcnt(2)
	v_mul_f32_e32 v79, 0x42b40000, v120
	s_waitcnt vmcnt(1)
	v_mul_f32_e32 v80, 0x42b40000, v124
	s_waitcnt vmcnt(0)
	v_mul_f32_e32 v81, 0x42b40000, v156
	v_mul_f32_e32 v133, 0x42b40000, v18
	v_mul_f32_e32 v136, 0x42b40000, v19
	v_mul_f32_e32 v19, 0x42b40000, v21
	v_mul_f32_e32 v21, 0x42b40000, v22
	v_mul_f32_e32 v22, 0x42b40000, v23
	v_mul_f32_e32 v23, 0x42b40000, v25
	v_mul_f32_e32 v25, 0x42b40000, v26
	v_mul_f32_e32 v26, 0x42b40000, v27
	v_mul_f32_e32 v27, 0x42b40000, v29
	v_mul_f32_e32 v29, 0x42b40000, v30
	v_mul_f32_e32 v30, 0x42b40000, v31
	v_mul_f32_e32 v31, 0x42b40000, v33
	v_mul_f32_e32 v33, 0x42b40000, v34
	v_mul_f32_e32 v40, 0x42b40000, v45
	v_mul_f32_e32 v45, 0x42b40000, v46
	v_mul_f32_e32 v46, 0x42b40000, v50
	v_mul_f32_e32 v162, 0x42b40000, v55
	v_mul_f32_e32 v64, 0x42b40000, v57
	v_mul_f32_e32 v167, 0x42b40000, v63
	v_mul_f32_e32 v65, 0x42b40000, v65
	v_mul_f32_e32 v168, 0x42b40000, v66
	v_mul_f32_e32 v169, 0x42b40000, v67
	v_mul_f32_e32 v55, 0x42b40000, v69
	v_mul_f32_e32 v170, 0x42b40000, v70
	v_mul_f32_e32 v171, 0x42b40000, v71
	v_mul_f32_e32 v57, 0x42b40000, v73
	v_mul_f32_e32 v172, 0x42b40000, v74
	v_mul_f32_e32 v173, 0x42b40000, v75
	v_mul_f32_e32 v176, 0x42b40000, v82
	v_mul_f32_e32 v177, 0x42b40000, v83
	v_mul_f32_e32 v63, 0x42b40000, v85
	v_mul_f32_e32 v104, 0x42b40000, v86
	v_mul_f32_e32 v178, 0x42b40000, v87
	v_mul_f32_e32 v87, 0x42b40000, v89
	v_mul_f32_e32 v108, 0x42b40000, v90
	v_mul_f32_e32 v179, 0x42b40000, v91
	v_mul_f32_e32 v88, 0x42b40000, v93
	v_mul_f32_e32 v112, 0x42b40000, v94
	v_mul_f32_e32 v180, 0x42b40000, v95
	v_mul_f32_e32 v89, 0x42b40000, v97
	v_mul_f32_e32 v116, 0x42b40000, v98
	v_mul_f32_e32 v181, 0x42b40000, v99
	v_mul_f32_e32 v90, 0x42b40000, v101
	v_mul_f32_e32 v120, 0x42b40000, v102
	v_mul_f32_e32 v182, 0x42b40000, v103
	v_mul_f32_e32 v91, 0x42b40000, v105
	v_mul_f32_e32 v124, 0x42b40000, v106
	v_mul_f32_e32 v183, 0x42b40000, v107
	v_mul_f32_e32 v92, 0x42b40000, v109
	v_mul_f32_e32 v109, 0x42b40000, v110
	v_mul_f32_e32 v156, 0x42b40000, v111
	v_mul_f32_e32 v93, 0x42b40000, v113
	v_mul_f32_e32 v94, 0x42b40000, v117
	v_mul_f32_e32 v110, 0x42b40000, v114
	v_mul_f32_e32 v184, 0x42b40000, v115
	v_mul_f32_e32 v95, 0x42b40000, v121
	v_mul_f32_e32 v96, 0x42b40000, v125
	v_mul_f32_e32 v111, 0x42b40000, v118
	v_mul_f32_e32 v185, 0x42b40000, v119
	v_mul_f32_e32 v97, 0x42b40000, v157
	v_mul_f32_e32 v113, 0x42b40000, v122
	v_mul_f32_e32 v114, 0x42b40000, v126
; template <int MODE>
; __device__ __forceinline__ void tr_matrix6(const float* W, int nb, int K, int N, unsigned char* WT, int drows, int rot, int gw, int NGW, int lane, float wscale) {
;     ...
;         for (int j = 0; j < 4; ++j) { float x[32];
; #pragma unroll
;             for (int i = 0; i < 32; ++i) x[i] = v[i][j] * wscale;
;             const v6u w = pk32_fp6(x);
;             *(u32x4*)(dst + (size_t)j * K) = (u32x4){w[0], w[1], w[2], w[3]}; *(u32x4*)(dst + (size_t)j * K + 16) = (u32x4){w[4], w[5], 0u, 0u}; }
	v_mul_f32_e32 v157, 0x42b40000, v123
	v_mul_f32_e32 v115, 0x42b40000, v158
	v_mul_f32_e32 v158, 0x42b40000, v127
	v_mul_f32_e32 v159, 0x42b40000, v159
	v_med3_f32 v50, v3, s45, v155
	v_med3_f32 v34, v4, s45, v155
	v_med3_f32 v18, v5, s45, v155
	v_med3_f32 v3, v6, s45, v155
	v_med3_f32 v66, v41, s45, v155
	v_med3_f32 v67, v43, s45, v155
	v_med3_f32 v4, v7, s45, v155
	v_med3_f32 v68, v51, s45, v155
	v_med3_f32 v5, v8, s45, v155
	v_med3_f32 v69, v52, s45, v155
	v_med3_f32 v6, v12, s45, v155
	v_med3_f32 v70, v53, s45, v155
	v_med3_f32 v7, v16, s45, v155
	v_med3_f32 v71, v54, s45, v155
	v_med3_f32 v8, v20, s45, v155
	v_med3_f32 v72, v56, s45, v155
	v_med3_f32 v9, v9, s45, v155
	v_med3_f32 v73, v58, s45, v155
	v_med3_f32 v10, v10, s45, v155
	v_med3_f32 v74, v60, s45, v155
	v_med3_f32 v11, v11, s45, v155
	v_med3_f32 v75, v62, s45, v155
	v_med3_f32 v12, v13, s45, v155
	v_med3_f32 v76, v76, s45, v155
	v_med3_f32 v13, v14, s45, v155
	v_med3_f32 v77, v77, s45, v155
	v_med3_f32 v14, v15, s45, v155
	v_med3_f32 v78, v78, s45, v155
	v_med3_f32 v15, v17, s45, v155
	v_med3_f32 v79, v79, s45, v155
	v_med3_f32 v16, v37, s45, v155
	v_med3_f32 v80, v80, s45, v155
	v_med3_f32 v17, v39, s45, v155
	v_med3_f32 v81, v81, s45, v155
	v_med3_f32 v51, v24, s45, v155
	v_med3_f32 v82, v55, s45, v155
	v_med3_f32 v83, v57, s45, v155
	v_med3_f32 v52, v32, s45, v155
	v_med3_f32 v84, v59, s45, v155
	v_med3_f32 v53, v36, s45, v155
	v_med3_f32 v85, v61, s45, v155
	v_med3_f32 v54, v19, s45, v155
	v_med3_f32 v86, v63, s45, v155
	v_med3_f32 v55, v23, s45, v155
	v_med3_f32 v87, v87, s45, v155
	v_med3_f32 v56, v27, s45, v155
	v_med3_f32 v88, v88, s45, v155
	v_med3_f32 v57, v31, s45, v155
	v_med3_f32 v89, v89, s45, v155
	v_med3_f32 v58, v35, s45, v155
	v_med3_f32 v90, v90, s45, v155
	v_med3_f32 v59, v38, s45, v155
	v_med3_f32 v91, v91, s45, v155
	v_med3_f32 v60, v40, s45, v155
	v_med3_f32 v92, v92, s45, v155
	v_med3_f32 v61, v42, s45, v155
	v_med3_f32 v93, v93, s45, v155
	v_med3_f32 v62, v47, s45, v155
	v_med3_f32 v94, v94, s45, v155
	v_med3_f32 v63, v64, s45, v155
	v_med3_f32 v95, v95, s45, v155
	v_med3_f32 v64, v165, s45, v155
	v_med3_f32 v96, v96, s45, v155
	v_med3_f32 v65, v65, s45, v155
	v_med3_f32 v97, v97, s45, v155
	v_med3_f32 v35, v28, s45, v155
	v_med3_f32 v98, v170, s45, v155
	v_med3_f32 v99, v172, s45, v155
	v_med3_f32 v36, v129, s45, v155
	v_med3_f32 v100, v174, s45, v155
	v_med3_f32 v37, v133, s45, v155
	v_med3_f32 v101, v176, s45, v155
	v_med3_f32 v38, v21, s45, v155
	v_med3_f32 v102, v104, s45, v155
	v_med3_f32 v39, v25, s45, v155
	v_med3_f32 v103, v108, s45, v155
	v_med3_f32 v40, v29, s45, v155
	v_med3_f32 v104, v112, s45, v155
	v_med3_f32 v41, v33, s45, v155
	v_med3_f32 v105, v116, s45, v155
	v_med3_f32 v42, v44, s45, v155
	v_med3_f32 v106, v120, s45, v155
	v_med3_f32 v43, v48, s45, v155
	v_med3_f32 v107, v124, s45, v155
	v_med3_f32 v44, v45, s45, v155
	v_med3_f32 v108, v109, s45, v155
	v_med3_f32 v45, v46, s45, v155
	v_med3_f32 v109, v110, s45, v155
	v_med3_f32 v46, v49, s45, v155
	v_med3_f32 v110, v111, s45, v155
	v_med3_f32 v47, v163, s45, v155
	v_med3_f32 v111, v113, s45, v155
	v_med3_f32 v48, v166, s45, v155
	v_med3_f32 v112, v114, s45, v155
	v_med3_f32 v49, v168, s45, v155
	v_med3_f32 v113, v115, s45, v155
	v_med3_f32 v19, v128, s45, v155
	v_med3_f32 v114, v171, s45, v155
	v_med3_f32 v115, v173, s45, v155
	v_med3_f32 v20, v132, s45, v155
	v_med3_f32 v116, v175, s45, v155
	v_med3_f32 v21, v136, s45, v155
	v_med3_f32 v117, v177, s45, v155
	v_med3_f32 v22, v22, s45, v155
	v_med3_f32 v118, v178, s45, v155
	v_med3_f32 v23, v26, s45, v155
	v_med3_f32 v119, v179, s45, v155
	v_med3_f32 v24, v30, s45, v155
	v_med3_f32 v120, v180, s45, v155
	v_med3_f32 v25, v137, s45, v155
	v_med3_f32 v121, v181, s45, v155
	v_med3_f32 v26, v140, s45, v155
	v_med3_f32 v122, v182, s45, v155
	v_med3_f32 v27, v141, s45, v155
	v_med3_f32 v123, v183, s45, v155
	v_med3_f32 v28, v160, s45, v155
	v_med3_f32 v124, v156, s45, v155
	v_med3_f32 v29, v161, s45, v155
	v_med3_f32 v125, v184, s45, v155
	v_med3_f32 v30, v162, s45, v155
	v_med3_f32 v126, v185, s45, v155
	v_med3_f32 v31, v164, s45, v155
	v_med3_f32 v127, v157, s45, v155
	v_med3_f32 v32, v167, s45, v155
	v_med3_f32 v128, v158, s45, v155
	v_med3_f32 v33, v169, s45, v155
	v_med3_f32 v129, v159, s45, v155
	v_cvt_scalef32_2xpk16_fp6_f32 v[2:7], v[2:17], v[66:81], 1.0
	v_cvt_scalef32_2xpk16_fp6_f32 v[8:13], v[50:65], v[82:97], 1.0
	v_cvt_scalef32_2xpk16_fp6_f32 v[34:39], v[34:49], v[98:113], 1.0
	v_cvt_scalef32_2xpk16_fp6_f32 v[14:19], v[18:33], v[114:129], 1.0
	v_mov_b32_e32 v128, v6
	v_mov_b32_e32 v129, v7
	global_store_dwordx4 v[150:151], v[2:5], off
	global_store_dwordx4 v[150:151], v[8:11], off offset:2048
	v_mov_b32_e32 v132, v12
	v_mov_b32_e32 v133, v13
	global_store_dwordx4 v[152:153], v[34:37], off
	v_mov_b32_e32 v136, v38
	v_mov_b32_e32 v137, v39
	global_store_dwordx4 v[152:153], v[14:17], off offset:2048
	v_mov_b32_e32 v140, v18
	v_mov_b32_e32 v141, v19
	global_store_dwordx4 v[150:151], v[128:131], off offset:16
	global_store_dwordx4 v[150:151], v[132:135], off offset:2064
	global_store_dwordx4 v[152:153], v[136:139], off offset:16
	global_store_dwordx4 v[152:153], v[140:143], off offset:2064
	s_cbranch_scc1 .LBB0_58

; #define RP(n) _Pragma("nounroll") for (int rep_ = 0; rep_ < (int)(((REPEAT) >> (n)) & 1u) + 1; ++rep_)
; __global__ void __launch_bounds__(NTHREADS, 2) fwd_kernel(Args args) {
;     ...
;     if (PH(15)) RP(15)
;     {
;         const int vcu = (G % 8 == 0) ? (bx % 8) * (G / 8) + bx / 8 : bx;
;         att::CvtState cs{args.in[I_MOED], ws + W_MOED, gw * att::CV_IPW, (gw + 1) * att::CV_IPW};
;         for (int L = vcu; L < NBATCH * NH * 8; L += G) {
.LBB0_1020:
	s_or_b64 exec, exec, s[4:5]
	s_lshr_b32 s0, s3, 29
	s_add_i32 s5, s2, s0
	s_and_b32 s0, s5, -8
	s_ashr_i32 s1, s76, 3
	s_sub_i32 s0, s2, s0
	s_mul_i32 s8, s1, s0
	s_ashr_i32 s1, s5, 3
	s_and_b32 s4, s76, 7
	s_add_i32 s5, s8, s1
	v_readlane_b32 s8, v251, 9
	s_add_u32 s30, s70, 0x24a00000
	s_mul_i32 s35, s8, 28
	s_addc_u32 s31, s71, 0
	s_add_i32 s50, s35, 28
	v_readlane_b32 s9, v251, 10
	s_add_u32 s8, s70, 0x4bc00000
	s_addc_u32 s9, s71, 0
	s_cmp_eq_u32 s4, 0
	s_cselect_b32 s51, s5, s2
	s_cmpk_gt_i32 s51, 0x1ff
	s_waitcnt lgkmcnt(0)
	s_barrier
	s_cbranch_scc1 .LBB0_1053
	s_add_u32 s4, s70, 0x3da00000
	s_addc_u32 s5, s71, 0
	s_add_u32 s10, s70, 0x3c200000
	s_addc_u32 s11, s71, 0
	s_movk_i32 s52, 0x2000
	s_mov_b32 s53, 0xc3e00000
	v_mov_b32_e32 v203, 0x43e00000
	v_mov_b32_e32 v191, 0
	s_movk_i32 s54, 0xd0
	s_movk_i32 s55, 0x3000
	s_mov_b32 s56, 0x5010400
	s_mov_b32 s57, 0x7030602
	s_mov_b32 s58, 0x5040100
	s_mov_b32 s59, 0x7060302
	s_add_i32 s60, 0, 0x6800
	s_movk_i32 s61, 0x1c00
	s_movk_i32 s62, 0x4000
	s_movk_i32 s63, 0x6000
	s_mov_b32 s64, 0x8000
	s_mov_b32 s65, 0xa000
	s_mov_b32 s66, 0xc000
	s_mov_b32 s67, 0xe000
	v_mov_b32_e32 v208, 0x1c00
	v_mov_b32_e32 v209, 0xff800000
	v_readlane_b32 s18, v251, 0
	v_readlane_b32 s19, v251, 1
	v_readlane_b32 s98, v251, 9
	s_nop 3
	s_sub_u32 s18, s18, 0x38
	s_subb_u32 s19, s19, 0
	s_load_dwordx4 s[44:47], s[18:19], 0x0
	s_mul_i32 s98, s98, 28
	s_add_i32 s99, s98, 28
	s_mov_b32 s100, 0
	s_waitcnt lgkmcnt(0)
	v_writelane_b32 v252, s44, 0
	v_writelane_b32 v252, s45, 1
	v_writelane_b32 v252, s46, 2
	v_writelane_b32 v252, s47, 3
	s_branch .LBB0_1023

; __device__ __forceinline__ void attn_unit(LAS unsigned char* lds, const unsigned char* Q, const unsigned char* KV, const bf16_t* KPE, const float* CST, bf16_t* O, int b, int h, int qb, CvtState& cs) {
;     ...
;     for (int t = 0; t < NT; ++t) {
;         if (t + 1 < NT) ATT_LOAD(t + 1);
.LBB0_1028:
	s_add_i32 s88, s89, 1
	s_cmp_lt_u32 s88, s33
	s_cselect_b64 s[44:45], -1, 0
	s_cmp_ge_u32 s88, s33
	s_cbranch_scc1 .LBB0_1043
	v_lshl_add_u64 v[74:75], s[12:13], 0, v[190:191]
	v_add_co_u32_e32 v74, vcc, 0x20000, v74
	s_waitcnt vmcnt(32)
	v_mov_b32_e32 v207, v191
	v_addc_co_u32_e32 v75, vcc, 0, v75, vcc
	global_load_dwordx2 v[196:197], v190, s[12:13]
	global_load_dwordx2 v[198:199], v[74:75], off
	global_load_dwordx4 v[154:157], v216, s[4:5]
	v_lshl_add_u64 v[74:75], s[12:13], 0, v[206:207]
	v_add_co_u32_e32 v76, vcc, 0x1000, v74
	global_load_dword v193, v206, s[12:13]
	s_nop 0
	v_addc_co_u32_e32 v77, vcc, 0, v75, vcc
	global_load_dword v195, v[76:77], off
	v_add_co_u32_e32 v76, vcc, 0x2000, v74
	s_nop 1
	v_addc_co_u32_e32 v77, vcc, 0, v75, vcc
	v_add_co_u32_e32 v74, vcc, 0x3000, v74
	global_load_dword v207, v[76:77], off
	s_nop 0
	v_addc_co_u32_e32 v75, vcc, 0, v75, vcc
	global_load_dword v211, v[74:75], off
	s_andn2_b64 vcc, exec, s[46:47]
	s_cbranch_vccz .LBB0_1044

; template <int MODE>
; __device__ __forceinline__ void tr_matrix6(const float* W, int nb, int K, int N, unsigned char* WT, int drows, int rot, int gw, int NGW, int lane, float wscale) {
;     ...
;     for (; it < total; it += NGW) {
;         const int e = it / per, r = it - e * per, kb = r / nbn, nbk = r - kb * nbn, n0 = nbk * 32, k0 = kb * 256;
;         const float* src = W + (size_t)e * K * N + (size_t)(k0 + 32 * q) * N + n0 + 4 * c;
;         f32x4 v[32];
; #pragma unroll
;         for (int i = 0; i < 32; ++i) v[i] = *(const f32x4*)(src + (size_t)i * N);
.LBB0_1037:
	s_and_b32 s18, s89, 3
	s_cmp_eq_u32 s18, 2
	s_cbranch_scc0 .Lf6_noload_a
	s_cmp_lt_i32 s98, s99
	s_cbranch_scc0 .Lf6_noload_a
	s_mul_hi_u32 s18, s98, 0x2492493
	s_mul_i32 s19, s18, 0x70
	s_sub_u32 s19, s98, s19
	s_and_b32 s20, s18, 63
	s_lshr_b32 s18, s18, 6
	s_and_b32 s21, s18, 3
	s_add_u32 s21, s21, 4
	s_lshr_b32 s18, s18, 2
	s_lshl_b32 s21, s21, 11
	s_lshl_b32 s20, s20, 5
	s_add_u32 s21, s21, s20
	s_mul_i32 s21, s21, 0x7000
	s_lshl_b32 s19, s19, 8
	s_add_u32 s21, s21, s19
	s_lshl_b32 s20, s18, 1
	s_nop 3
	v_readlane_b32 s18, v252, s20
	s_add_u32 s20, s20, 1
	s_nop 3
	v_readlane_b32 s19, v252, s20
	s_nop 3
	s_add_u32 s18, s18, s21
	s_addc_u32 s19, s19, 0
	v_mbcnt_lo_u32_b32 v218, -1, 0
	v_mbcnt_hi_u32_b32 v218, -1, v218
	v_lshlrev_b32_e32 v218, 2, v218
	global_load_dword v158, v218, s[18:19]
	s_add_u32 s18, s18, 0x7000
	s_addc_u32 s19, s19, 0
	global_load_dword v159, v218, s[18:19]
	s_add_u32 s18, s18, 0x7000
	s_addc_u32 s19, s19, 0
	global_load_dword v160, v218, s[18:19]
	s_add_u32 s18, s18, 0x7000
	s_addc_u32 s19, s19, 0
	global_load_dword v161, v218, s[18:19]
	s_add_u32 s18, s18, 0x7000
	s_addc_u32 s19, s19, 0
	global_load_dword v162, v218, s[18:19]
	s_add_u32 s18, s18, 0x7000
	s_addc_u32 s19, s19, 0
	global_load_dword v163, v218, s[18:19]
	s_add_u32 s18, s18, 0x7000
	s_addc_u32 s19, s19, 0
	global_load_dword v164, v218, s[18:19]
	s_add_u32 s18, s18, 0x7000
	s_addc_u32 s19, s19, 0
	global_load_dword v165, v218, s[18:19]
	s_add_u32 s18, s18, 0x7000
	s_addc_u32 s19, s19, 0
	global_load_dword v166, v218, s[18:19]
	s_add_u32 s18, s18, 0x7000
	s_addc_u32 s19, s19, 0
	global_load_dword v167, v218, s[18:19]
	s_add_u32 s18, s18, 0x7000
	s_addc_u32 s19, s19, 0
	global_load_dword v168, v218, s[18:19]
	s_add_u32 s18, s18, 0x7000
	s_addc_u32 s19, s19, 0
	global_load_dword v169, v218, s[18:19]
	s_add_u32 s18, s18, 0x7000
	s_addc_u32 s19, s19, 0
	global_load_dword v170, v218, s[18:19]
	s_add_u32 s18, s18, 0x7000
	s_addc_u32 s19, s19, 0
	global_load_dword v171, v218, s[18:19]
	s_add_u32 s18, s18, 0x7000
	s_addc_u32 s19, s19, 0
	global_load_dword v172, v218, s[18:19]
	s_add_u32 s18, s18, 0x7000
	s_addc_u32 s19, s19, 0
	global_load_dword v173, v218, s[18:19]
	s_add_u32 s18, s18, 0x7000
	s_addc_u32 s19, s19, 0
	global_load_dword v174, v218, s[18:19]
	s_add_u32 s18, s18, 0x7000
	s_addc_u32 s19, s19, 0
	global_load_dword v175, v218, s[18:19]
	s_add_u32 s18, s18, 0x7000
	s_addc_u32 s19, s19, 0
	global_load_dword v176, v218, s[18:19]
	s_add_u32 s18, s18, 0x7000
	s_addc_u32 s19, s19, 0
	global_load_dword v177, v218, s[18:19]
	s_add_u32 s18, s18, 0x7000
	s_addc_u32 s19, s19, 0
	global_load_dword v178, v218, s[18:19]
	s_add_u32 s18, s18, 0x7000
	s_addc_u32 s19, s19, 0
	global_load_dword v179, v218, s[18:19]
	s_add_u32 s18, s18, 0x7000
	s_addc_u32 s19, s19, 0
	global_load_dword v180, v218, s[18:19]
	s_add_u32 s18, s18, 0x7000
	s_addc_u32 s19, s19, 0
	global_load_dword v181, v218, s[18:19]
	s_add_u32 s18, s18, 0x7000
	s_addc_u32 s19, s19, 0
	global_load_dword v182, v218, s[18:19]
	s_add_u32 s18, s18, 0x7000
	s_addc_u32 s19, s19, 0
	global_load_dword v183, v218, s[18:19]
	s_add_u32 s18, s18, 0x7000
	s_addc_u32 s19, s19, 0
	global_load_dword v184, v218, s[18:19]
	s_add_u32 s18, s18, 0x7000
	s_addc_u32 s19, s19, 0
	global_load_dword v185, v218, s[18:19]
	s_add_u32 s18, s18, 0x7000
	s_addc_u32 s19, s19, 0
	global_load_dword v186, v218, s[18:19]
	s_add_u32 s18, s18, 0x7000
	s_addc_u32 s19, s19, 0
	global_load_dword v187, v218, s[18:19]
	s_add_u32 s18, s18, 0x7000
	s_addc_u32 s19, s19, 0
	global_load_dword v188, v218, s[18:19]
	s_add_u32 s18, s18, 0x7000
	s_addc_u32 s19, s19, 0
	global_load_dword v189, v218, s[18:19]
	s_mov_b32 s100, 1

; __device__ __forceinline__ v6u pk32_fp6(const float (&x)[32]) {
;     v16f a, b;
; #pragma unroll
;     for (int i = 0; i < 16; ++i) { a[i] = __builtin_amdgcn_fmed3f(x[i], -7.5f, 7.5f); b[i] = __builtin_amdgcn_fmed3f(x[16 + i], -7.5f, 7.5f); }
;     return __builtin_amdgcn_cvt_scalef32_2xpk16_fp6_f32(a, b, 1.0f);
; }
; template <int MODE>
; __device__ __forceinline__ void tr_matrix6(const float* W, int nb, int K, int N, unsigned char* WT, int drows, int rot, int gw, int NGW, int lane, float wscale) {
;     ...
;         const int drow0 = (MODE == 0) ? n0 : ((n0 >> 7) * 256 + (n0 & 127) + (MODE == 2 ? 128 : 0));
;         unsigned char* dst = WT + (size_t)e * drows * K + (size_t)(drow0 + 4 * c) * K + k0 + 32 * q;
; #pragma unroll
;         for (int j = 0; j < 4; ++j) { float x[32];
; #pragma unroll
;             for (int i = 0; i < 32; ++i) x[i] = v[i][j] * wscale;
;             const v6u w = pk32_fp6(x);
;             *(u32x4*)(dst + (size_t)j * K) = (u32x4){w[0], w[1], w[2], w[3]}; *(u32x4*)(dst + (size_t)j * K + 16) = (u32x4){w[4], w[5], 0u, 0u}; }
.LBB0_1047:
	s_cmp_lg_u32 s100, 0
	s_cbranch_scc0 .Lf6_nostore
	s_and_b32 s18, s89, 3
	s_cmp_eq_u32 s18, 3
	s_cbranch_scc0 .Lf6_nostore
	s_mul_hi_u32 s18, s98, 0x2492493
	s_mul_i32 s19, s18, 0x70
	s_sub_u32 s19, s98, s19
	s_and_b32 s20, s18, 63
	s_lshr_b32 s18, s18, 6
	s_and_b32 s21, s18, 3
	s_add_u32 s21, s21, 4
	s_lshr_b32 s18, s18, 2
	s_lshr_b32 s101, s19, 1
	s_lshl_b32 s101, s101, 8
	s_and_b32 s19, s19, 1
	s_lshl_b32 s19, s19, 6
	s_add_u32 s19, s19, s101
	s_lshl_b32 s18, s18, 7
	s_add_u32 s19, s19, s18
	s_mul_i32 s21, s21, 0x3800
	s_add_u32 s19, s19, s21
	s_lshl_b32 s19, s19, 11
	s_lshl_b32 s20, s20, 5
	s_add_u32 s19, s19, s20
	s_add_u32 s19, s19, 0x8a00000
	s_add_u32 s20, s70, s19
	s_addc_u32 s21, s71, 0
	v_mbcnt_lo_u32_b32 v218, -1, 0
	v_mbcnt_hi_u32_b32 v218, -1, v218
	v_lshlrev_b32_e32 v218, 11, v218
	v_mov_b32_e32 v219, 0x40f00000
	s_mov_b32 s18, 0xc0f00000
	v_mov_b32_e32 v80, 0
	v_mov_b32_e32 v81, 0
	s_waitcnt vmcnt(0)
	v_mul_f32_e32 v158, 0x42b40000, v158
	v_mul_f32_e32 v159, 0x42b40000, v159
	v_mul_f32_e32 v160, 0x42b40000, v160
	v_mul_f32_e32 v161, 0x42b40000, v161
	v_mul_f32_e32 v162, 0x42b40000, v162
	v_mul_f32_e32 v163, 0x42b40000, v163
	v_mul_f32_e32 v164, 0x42b40000, v164
	v_mul_f32_e32 v165, 0x42b40000, v165
	v_mul_f32_e32 v166, 0x42b40000, v166
	v_mul_f32_e32 v167, 0x42b40000, v167
	v_mul_f32_e32 v168, 0x42b40000, v168
	v_mul_f32_e32 v169, 0x42b40000, v169
	v_mul_f32_e32 v170, 0x42b40000, v170
	v_mul_f32_e32 v171, 0x42b40000, v171
	v_mul_f32_e32 v172, 0x42b40000, v172
	v_mul_f32_e32 v173, 0x42b40000, v173
	v_mul_f32_e32 v174, 0x42b40000, v174
	v_mul_f32_e32 v175, 0x42b40000, v175
	v_mul_f32_e32 v176, 0x42b40000, v176
	v_mul_f32_e32 v177, 0x42b40000, v177
	v_mul_f32_e32 v178, 0x42b40000, v178
	v_mul_f32_e32 v179, 0x42b40000, v179
	v_mul_f32_e32 v180, 0x42b40000, v180
	v_mul_f32_e32 v181, 0x42b40000, v181
	v_mul_f32_e32 v182, 0x42b40000, v182
	v_mul_f32_e32 v183, 0x42b40000, v183
	v_mul_f32_e32 v184, 0x42b40000, v184
	v_mul_f32_e32 v185, 0x42b40000, v185
	v_mul_f32_e32 v186, 0x42b40000, v186
	v_mul_f32_e32 v187, 0x42b40000, v187
	v_mul_f32_e32 v188, 0x42b40000, v188
	v_mul_f32_e32 v189, 0x42b40000, v189
	v_med3_f32 v158, v158, s18, v219
	v_med3_f32 v159, v159, s18, v219
	v_med3_f32 v160, v160, s18, v219
	v_med3_f32 v161, v161, s18, v219
	v_med3_f32 v162, v162, s18, v219
	v_med3_f32 v163, v163, s18, v219
	v_med3_f32 v164, v164, s18, v219
	v_med3_f32 v165, v165, s18, v219
	v_med3_f32 v166, v166, s18, v219
	v_med3_f32 v167, v167, s18, v219
	v_med3_f32 v168, v168, s18, v219
	v_med3_f32 v169, v169, s18, v219
	v_med3_f32 v170, v170, s18, v219
	v_med3_f32 v171, v171, s18, v219
	v_med3_f32 v172, v172, s18, v219
	v_med3_f32 v173, v173, s18, v219
	v_med3_f32 v174, v174, s18, v219
	v_med3_f32 v175, v175, s18, v219
	v_med3_f32 v176, v176, s18, v219
	v_med3_f32 v177, v177, s18, v219
	v_med3_f32 v178, v178, s18, v219
	v_med3_f32 v179, v179, s18, v219
	v_med3_f32 v180, v180, s18, v219
	v_med3_f32 v181, v181, s18, v219
	v_med3_f32 v182, v182, s18, v219
	v_med3_f32 v183, v183, s18, v219
	v_med3_f32 v184, v184, s18, v219
	v_med3_f32 v185, v185, s18, v219
	v_med3_f32 v186, v186, s18, v219
	v_med3_f32 v187, v187, s18, v219
	v_med3_f32 v188, v188, s18, v219
	v_med3_f32 v189, v189, s18, v219
	v_cvt_scalef32_2xpk16_fp6_f32 v[74:79], v[158:173], v[174:189], 1.0
	s_nop 1
	global_store_dwordx4 v218, v[74:77], s[20:21]
	global_store_dwordx4 v218, v[78:81], s[20:21] offset:16
	s_add_i32 s98, s98, 1
	s_mov_b32 s100, 0

.Lmy_attw_plain:
	s_cmp_lg_u32 s100, 0
	s_cbranch_scc0 .Lmy_attw_plain2
	s_bitcmp1_b32 s88, 0
	s_cselect_b32 s18, 0x3400, 0
	s_add_i32 s18, s18, 0
	v_add_u32_e32 v74, s18, v194
	s_waitcnt vmcnt(37)
	ds_write2st64_b64 v74, v[196:197], v[198:199] offset1:13
	v_mov_b32_e32 v74, v191
	v_mov_b32_e32 v75, v191
	s_waitcnt vmcnt(36)
	v_cvt_scalef32_pk_fp8_bf16 v74, v154, 1.0
	v_cvt_scalef32_pk_fp8_bf16 v75, v156, 1.0
	s_mul_i32 s19, s79, 0x2800
	v_cvt_scalef32_pk_fp8_bf16 v74, v155, 1.0 op_sel:[0,0,1]
	v_cvt_scalef32_pk_fp8_bf16 v75, v157, 1.0 op_sel:[0,0,1]
	v_add_u32_e32 v76, s18, v200
	ds_write_b64 v76, v[74:75] offset:128
	s_waitcnt vmcnt(34)
	v_perm_b32 v74, v195, v193, s56
	s_waitcnt vmcnt(32)
	v_perm_b32 v75, v211, v207, s56
	s_branch .Lmy_attw_join

; template <int MODE>
; __device__ __forceinline__ void tr_matrix6(const float* W, int nb, int K, int N, unsigned char* WT, int drows, int rot, int gw, int NGW, int lane, float wscale) {
;     ...
;     for (; it < total; it += NGW) {
;         const int e = it / per, r = it - e * per, kb = r / nbn, nbk = r - kb * nbn, n0 = nbk * 32, k0 = kb * 256;
;         const float* src = W + (size_t)e * K * N + (size_t)(k0 + 32 * q) * N + n0 + 4 * c;
;         f32x4 v[32];
; #pragma unroll
;         for (int i = 0; i < 32; ++i) v[i] = *(const f32x4*)(src + (size_t)i * N);
.LBB0_1049:
	s_and_b32 s18, s89, 3
	s_cmp_eq_u32 s18, 2
	s_cbranch_scc0 .Lf6_noload_b
	s_cmp_lt_i32 s98, s99
	s_cbranch_scc0 .Lf6_noload_b
	s_cmp_lg_u32 s100, 0
	s_cbranch_scc1 .Lf6_noload_b
	s_mul_hi_u32 s18, s98, 0x2492493
	s_mul_i32 s19, s18, 0x70
	s_sub_u32 s19, s98, s19
	s_and_b32 s20, s18, 63
	s_lshr_b32 s18, s18, 6
	s_and_b32 s21, s18, 3
	s_add_u32 s21, s21, 4
	s_lshr_b32 s18, s18, 2
	s_lshl_b32 s21, s21, 11
	s_lshl_b32 s20, s20, 5
	s_add_u32 s21, s21, s20
	s_mul_i32 s21, s21, 0x7000
	s_lshl_b32 s19, s19, 8
	s_add_u32 s21, s21, s19
	s_lshl_b32 s20, s18, 1
	s_nop 3
	v_readlane_b32 s18, v252, s20
	s_add_u32 s20, s20, 1
	s_nop 3
	v_readlane_b32 s19, v252, s20
	s_nop 3
	s_add_u32 s18, s18, s21
	s_addc_u32 s19, s19, 0
	v_mbcnt_lo_u32_b32 v218, -1, 0
	v_mbcnt_hi_u32_b32 v218, -1, v218
	v_lshlrev_b32_e32 v218, 2, v218
	global_load_dword v158, v218, s[18:19]
	s_add_u32 s18, s18, 0x7000
	s_addc_u32 s19, s19, 0
	global_load_dword v159, v218, s[18:19]
	s_add_u32 s18, s18, 0x7000
	s_addc_u32 s19, s19, 0
	global_load_dword v160, v218, s[18:19]
	s_add_u32 s18, s18, 0x7000
	s_addc_u32 s19, s19, 0
	global_load_dword v161, v218, s[18:19]
	s_add_u32 s18, s18, 0x7000
	s_addc_u32 s19, s19, 0
	global_load_dword v162, v218, s[18:19]
	s_add_u32 s18, s18, 0x7000
	s_addc_u32 s19, s19, 0
	global_load_dword v163, v218, s[18:19]
	s_add_u32 s18, s18, 0x7000
	s_addc_u32 s19, s19, 0
	global_load_dword v164, v218, s[18:19]
	s_add_u32 s18, s18, 0x7000
	s_addc_u32 s19, s19, 0
	global_load_dword v165, v218, s[18:19]
	s_add_u32 s18, s18, 0x7000
	s_addc_u32 s19, s19, 0
	global_load_dword v166, v218, s[18:19]
	s_add_u32 s18, s18, 0x7000
	s_addc_u32 s19, s19, 0
	global_load_dword v167, v218, s[18:19]
	s_add_u32 s18, s18, 0x7000
	s_addc_u32 s19, s19, 0
	global_load_dword v168, v218, s[18:19]
	s_add_u32 s18, s18, 0x7000
	s_addc_u32 s19, s19, 0
	global_load_dword v169, v218, s[18:19]
	s_add_u32 s18, s18, 0x7000
	s_addc_u32 s19, s19, 0
	global_load_dword v170, v218, s[18:19]
	s_add_u32 s18, s18, 0x7000
	s_addc_u32 s19, s19, 0
	global_load_dword v171, v218, s[18:19]
	s_add_u32 s18, s18, 0x7000
	s_addc_u32 s19, s19, 0
	global_load_dword v172, v218, s[18:19]
	s_add_u32 s18, s18, 0x7000
	s_addc_u32 s19, s19, 0
	global_load_dword v173, v218, s[18:19]
	s_add_u32 s18, s18, 0x7000
	s_addc_u32 s19, s19, 0
	global_load_dword v174, v218, s[18:19]
	s_add_u32 s18, s18, 0x7000
	s_addc_u32 s19, s19, 0
	global_load_dword v175, v218, s[18:19]
	s_add_u32 s18, s18, 0x7000
	s_addc_u32 s19, s19, 0
	global_load_dword v176, v218, s[18:19]
	s_add_u32 s18, s18, 0x7000
	s_addc_u32 s19, s19, 0
	global_load_dword v177, v218, s[18:19]
	s_add_u32 s18, s18, 0x7000
	s_addc_u32 s19, s19, 0
	global_load_dword v178, v218, s[18:19]
	s_add_u32 s18, s18, 0x7000
	s_addc_u32 s19, s19, 0
	global_load_dword v179, v218, s[18:19]
	s_add_u32 s18, s18, 0x7000
	s_addc_u32 s19, s19, 0
	global_load_dword v180, v218, s[18:19]
	s_add_u32 s18, s18, 0x7000
	s_addc_u32 s19, s19, 0
	global_load_dword v181, v218, s[18:19]
	s_add_u32 s18, s18, 0x7000
	s_addc_u32 s19, s19, 0
	global_load_dword v182, v218, s[18:19]
	s_add_u32 s18, s18, 0x7000
	s_addc_u32 s19, s19, 0
	global_load_dword v183, v218, s[18:19]
	s_add_u32 s18, s18, 0x7000
	s_addc_u32 s19, s19, 0
	global_load_dword v184, v218, s[18:19]
	s_add_u32 s18, s18, 0x7000
	s_addc_u32 s19, s19, 0
	global_load_dword v185, v218, s[18:19]
	s_add_u32 s18, s18, 0x7000
	s_addc_u32 s19, s19, 0
	global_load_dword v186, v218, s[18:19]
	s_add_u32 s18, s18, 0x7000
	s_addc_u32 s19, s19, 0
	global_load_dword v187, v218, s[18:19]
	s_add_u32 s18, s18, 0x7000
	s_addc_u32 s19, s19, 0
	global_load_dword v188, v218, s[18:19]
	s_add_u32 s18, s18, 0x7000
	s_addc_u32 s19, s19, 0
	global_load_dword v189, v218, s[18:19]
	s_mov_b32 s100, 1

; __global__ void __launch_bounds__(NTHREADS, 2) fwd_kernel(Args args) {
	.amdhsa_kernel _Z10fwd_kernel4Args
		.amdhsa_group_segment_fixed_size 0
		.amdhsa_private_segment_fixed_size 0
		.amdhsa_kernarg_size 512
		.amdhsa_user_sgpr_count 2
		.amdhsa_user_sgpr_dispatch_ptr 0
		.amdhsa_user_sgpr_queue_ptr 0
		.amdhsa_user_sgpr_kernarg_segment_ptr 1
		.amdhsa_user_sgpr_dispatch_id 0
		.amdhsa_user_sgpr_kernarg_preload_length 0
		.amdhsa_user_sgpr_kernarg_preload_offset 0
		.amdhsa_user_sgpr_private_segment_size 0
		.amdhsa_uses_dynamic_stack 0
		.amdhsa_enable_private_segment 0
		.amdhsa_system_sgpr_workgroup_id_x 1
		.amdhsa_system_sgpr_workgroup_id_y 0
		.amdhsa_system_sgpr_workgroup_id_z 0
		.amdhsa_system_sgpr_workgroup_info 0
		.amdhsa_system_vgpr_workitem_id 0
		.amdhsa_next_free_vgpr 256
		.amdhsa_next_free_sgpr 102
		.amdhsa_accum_offset 256
		.amdhsa_reserve_vcc 1
		.amdhsa_float_round_mode_32 0
		.amdhsa_float_round_mode_16_64 0
		.amdhsa_float_denorm_mode_32 3
		.amdhsa_float_denorm_mode_16_64 3
		.amdhsa_dx10_clamp 1
		.amdhsa_ieee_mode 1
		.amdhsa_fp16_overflow 0
		.amdhsa_tg_split 0
		.amdhsa_exception_fp_ieee_invalid_op 0
		.amdhsa_exception_fp_denorm_src 0
		.amdhsa_exception_fp_ieee_div_zero 0
		.amdhsa_exception_fp_ieee_overflow 0
		.amdhsa_exception_fp_ieee_underflow 0
		.amdhsa_exception_fp_ieee_inexact 0
		.amdhsa_exception_int_div_zero 0
	.end_amdhsa_kernel

; __global__ void __launch_bounds__(NTHREADS, 2) fwd_kernel(Args args) {
amdhsa.kernels:
  - .agpr_count:     0
    .args:
      - .offset:         0
        .size:           256
        .value_kind:     by_value
      - .offset:         256
        .size:           4
        .value_kind:     hidden_block_count_x
      - .offset:         260
        .size:           4
        .value_kind:     hidden_block_count_y
      - .offset:         264
        .size:           4
        .value_kind:     hidden_block_count_z
      - .offset:         268
        .size:           2
        .value_kind:     hidden_group_size_x
      - .offset:         270
        .size:           2
        .value_kind:     hidden_group_size_y
      - .offset:         272
        .size:           2
        .value_kind:     hidden_group_size_z
      - .offset:         274
        .size:           2
        .value_kind:     hidden_remainder_x
      - .offset:         276
        .size:           2
        .value_kind:     hidden_remainder_y
      - .offset:         278
        .size:           2
        .value_kind:     hidden_remainder_z
      - .offset:         296
        .size:           8
        .value_kind:     hidden_global_offset_x
      - .offset:         304
        .size:           8
        .value_kind:     hidden_global_offset_y
      - .offset:         312
        .size:           8
        .value_kind:     hidden_global_offset_z
      - .offset:         320
        .size:           2
        .value_kind:     hidden_grid_dims
      - .offset:         376
        .size:           4
        .value_kind:     hidden_dynamic_lds_size
    .group_segment_fixed_size: 0
    .kernarg_segment_align: 8
    .kernarg_segment_size: 512
    .language:       OpenCL C
    .language_version:
      - 2
      - 0
    .max_flat_workgroup_size: 512
    .name:           _Z10fwd_kernel4Args
    .private_segment_fixed_size: 0
    .sgpr_count:     108
    .sgpr_spill_count: 86
    .symbol:         _Z10fwd_kernel4Args.kd
    .uniform_work_group_size: 1
    .uses_dynamic_stack: false
    .vgpr_count:     256
    .vgpr_spill_count: 0
    .wavefront_size: 64
